# attention block selection: top-13 threshold search loop keeps threshold and bit index in SGPRs (scalar candidate, vector compares, scalar counts)
# speedup vs baseline: 1.0078x; 1.0078x over previous
.LBB0_1006:
	s_add_i32 s0, s14, s16
	v_or_b32_e32 v4, s0, v230
	v_ashrrev_i32_e32 v5, 31, v4
	v_lshlrev_b64 v[186:187], 13, v[4:5]
	v_lshl_add_u64 v[118:119], s[96:97], 0, v[186:187]
	v_lshlrev_b32_e32 v2, 2, v178
	v_readlane_b32 s0, v255, 5
	v_mul_u32_u24_e32 v1, 3, v175
	v_lshl_add_u64 v[118:119], v[118:119], 0, v[2:3]
	v_mov_b32_e32 v175, v3
	v_readlane_b32 s1, v255, 6
	v_lshl_add_u64 v[182:183], v[118:119], 0, v[174:175]
	s_movk_i32 s6, 0xc0
	v_mov_b64_e32 v[118:119], s[0:1]
	v_mad_i64_i32 v[120:121], s[0:1], v4, s6, v[118:119]
	v_lshlrev_b32_e32 v122, 2, v1
	v_mov_b32_e32 v123, v3
	v_lshl_add_u64 v[190:191], v[120:121], 0, v[122:123]
	global_load_dword v120, v[190:191], off
	v_or_b32_e32 v4, 4, v4
	v_ashrrev_i32_e32 v5, 31, v4
	v_lshlrev_b64 v[188:189], 13, v[4:5]
	v_mad_i64_i32 v[4:5], s[0:1], v4, s6, v[118:119]
	v_lshl_add_u64 v[192:193], v[4:5], 0, v[122:123]
	s_ashr_i32 s6, s14, 6
	s_cmp_gt_i32 s6, 15
	s_cselect_b64 s[34:35], -1, 0
	s_add_i32 s0, s6, -2
	v_readlane_b32 s8, v255, 15
	v_cmp_ge_i32_e32 vcc, s0, v166
	v_readlane_b32 s9, v255, 16
	v_cmp_ge_i32_e64 s[24:25], s0, v214
	v_readlane_b32 s0, v255, 17
	s_and_b64 s[92:93], s[8:9], vcc
	v_cmp_eq_u32_e32 vcc, s6, v166
	v_readlane_b32 s1, v255, 18
	s_or_b64 s[0:1], s[0:1], vcc
	s_xor_b64 s[88:89], s[0:1], -1
	s_add_i32 s0, s6, -1
	v_cmp_eq_u32_e64 s[22:23], s0, v166
	v_cmp_eq_u32_e64 s[20:21], s6, v214
	s_add_i32 s0, s6, 0xffffffbf
	s_add_i32 s6, s6, 1
	v_cmp_eq_u32_e64 s[18:19], s0, v166
	s_lshl_b64 s[0:1], -1, s6
	s_mov_b64 s[94:95], 0
	s_and_b64 vcc, exec, s[34:35]
	s_waitcnt vmcnt(0)
	v_pk_mul_f32 v[116:117], v[116:117], v[120:121] op_sel_hi:[1,0]
	v_pk_mul_f32 v[114:115], v[114:115], v[120:121] op_sel_hi:[1,0]
	v_pk_mul_f32 v[112:113], v[112:113], v[120:121] op_sel_hi:[1,0]
	v_pk_mul_f32 v[110:111], v[110:111], v[120:121] op_sel_hi:[1,0]
	v_pk_mul_f32 v[108:109], v[108:109], v[120:121] op_sel_hi:[1,0]
	v_pk_mul_f32 v[106:107], v[106:107], v[120:121] op_sel_hi:[1,0]
	v_pk_mul_f32 v[104:105], v[104:105], v[120:121] op_sel_hi:[1,0]
	v_pk_mul_f32 v[102:103], v[102:103], v[120:121] op_sel_hi:[1,0]
	v_pk_mul_f32 v[100:101], v[100:101], v[120:121] op_sel_hi:[1,0]
	v_pk_mul_f32 v[98:99], v[98:99], v[120:121] op_sel_hi:[1,0]
	v_pk_mul_f32 v[96:97], v[96:97], v[120:121] op_sel_hi:[1,0]
	v_pk_mul_f32 v[94:95], v[94:95], v[120:121] op_sel_hi:[1,0]
	v_pk_mul_f32 v[92:93], v[92:93], v[120:121] op_sel_hi:[1,0]
	v_pk_mul_f32 v[90:91], v[90:91], v[120:121] op_sel_hi:[1,0]
	v_pk_mul_f32 v[88:89], v[88:89], v[120:121] op_sel_hi:[1,0]
	v_pk_mul_f32 v[86:87], v[86:87], v[120:121] op_sel_hi:[1,0]
	global_store_dwordx4 v[182:183], v[114:117], off
	global_store_dwordx4 v[182:183], v[110:113], off offset:64
	global_store_dwordx4 v[182:183], v[106:109], off offset:128
	global_store_dwordx4 v[182:183], v[102:105], off offset:192
	global_store_dwordx4 v[182:183], v[98:101], off offset:256
	global_store_dwordx4 v[182:183], v[94:97], off offset:320
	global_store_dwordx4 v[182:183], v[90:93], off offset:384
	global_store_dwordx4 v[182:183], v[86:89], off offset:448
	s_nop 1
	v_lshl_add_u64 v[86:87], s[96:97], 0, v[188:189]
	v_lshl_add_u64 v[86:87], v[86:87], 0, v[2:3]
	global_load_dword v2, v[192:193], off
	v_lshl_add_u64 v[184:185], v[86:87], 0, v[174:175]
	s_not_b64 s[96:97], s[0:1]
	s_mov_b64 s[42:43], s[96:97]
	s_waitcnt vmcnt(0)
	v_pk_mul_f32 v[56:57], v[56:57], v[2:3] op_sel_hi:[1,0]
	v_pk_mul_f32 v[54:55], v[54:55], v[2:3] op_sel_hi:[1,0]
	global_store_dwordx4 v[184:185], v[54:57], off offset:192
	v_pk_mul_f32 v[72:73], v[72:73], v[2:3] op_sel_hi:[1,0]
	v_pk_mul_f32 v[70:71], v[70:71], v[2:3] op_sel_hi:[1,0]
	v_pk_mul_f32 v[56:57], v[84:85], v[2:3] op_sel_hi:[1,0]
	v_pk_mul_f32 v[54:55], v[82:83], v[2:3] op_sel_hi:[1,0]
	global_store_dwordx4 v[184:185], v[54:57], off offset:256
	v_pk_mul_f32 v[64:65], v[64:65], v[2:3] op_sel_hi:[1,0]
	v_pk_mul_f32 v[62:63], v[62:63], v[2:3] op_sel_hi:[1,0]
	v_pk_mul_f32 v[56:57], v[80:81], v[2:3] op_sel_hi:[1,0]
	v_pk_mul_f32 v[54:55], v[78:79], v[2:3] op_sel_hi:[1,0]
	global_store_dwordx4 v[184:185], v[54:57], off offset:320
	v_pk_mul_f32 v[60:61], v[60:61], v[2:3] op_sel_hi:[1,0]
	v_pk_mul_f32 v[58:59], v[58:59], v[2:3] op_sel_hi:[1,0]
	v_pk_mul_f32 v[56:57], v[76:77], v[2:3] op_sel_hi:[1,0]
	v_pk_mul_f32 v[54:55], v[74:75], v[2:3] op_sel_hi:[1,0]
	global_store_dwordx4 v[184:185], v[54:57], off offset:384
	global_store_dwordx4 v[184:185], v[70:73], off
	global_store_dwordx4 v[184:185], v[62:65], off offset:64
	v_pk_mul_f32 v[56:57], v[68:69], v[2:3] op_sel_hi:[1,0]
	v_pk_mul_f32 v[54:55], v[66:67], v[2:3] op_sel_hi:[1,0]
	global_store_dwordx4 v[184:185], v[58:61], off offset:128
	global_store_dwordx4 v[184:185], v[54:57], off offset:448
	s_waitcnt lgkmcnt(0)
	s_cbranch_vccz .LBB0_1020
	v_mov_b32_e32 v1, -1
	v_mov_b32_e32 v2, -1
	s_and_saveexec_b64 s[0:1], s[92:93]
	ds_read_b32 v2, v215 offset:8192
	s_or_b64 exec, exec, s[0:1]
	s_and_saveexec_b64 s[0:1], s[24:25]
	ds_read_b32 v1, v215 offset:8448
	s_or_b64 exec, exec, s[0:1]
	v_mov_b32_e32 v5, 30
	v_mov_b32_e32 v4, 0
	s_mov_b32 s98, 0
	s_mov_b32 s99, 30
	s_waitcnt lgkmcnt(0)
.LBB0_1012:
	s_lshl_b32 s100, 1, s99
	s_or_b32 s100, s100, s98
	v_cmp_le_i32_e32 vcc, s100, v2
	v_cmp_le_i32_e64 s[0:1], s100, v1
	s_bcnt1_i32_b64 s101, vcc
	s_bcnt1_i32_b64 s0, s[0:1]
	s_add_i32 s101, s101, s0
	s_cmp_ge_u32 s101, 13
	s_cselect_b32 s98, s100, s98
	s_cmp_eq_u32 s101, 13
	s_cbranch_scc1 .Ltk_done_0
	s_sub_i32 s99, s99, 1
	s_cmp_ge_i32 s99, 0
	s_cbranch_scc1 .LBB0_1012
.Ltk_done_0:
	v_mov_b32_e32 v4, s98
	v_cmp_gt_i32_e64 s[26:27], v2, v4
	s_bcnt1_i32_b64 s6, s[26:27]
	v_cmp_gt_i32_e64 s[26:27], v1, v4
	s_bcnt1_i32_b64 s7, s[26:27]
	s_add_i32 s6, s6, s7
	v_cmp_ne_u32_e64 s[0:1], v2, v4
	v_cmp_eq_u32_e64 s[28:29], v2, v4
	v_cmp_eq_u32_e32 vcc, v1, v4
	v_cmp_le_i32_e64 s[30:31], v2, v4
	s_sub_i32 s42, 13, s6
	s_mov_b64 s[6:7], -1
	s_and_saveexec_b64 s[36:37], s[30:31]
	s_cbranch_execz .LBB0_1019
	s_mov_b64 s[6:7], 0
	s_and_saveexec_b64 s[8:9], s[0:1]
	s_xor_b64 s[0:1], exec, s[8:9]
	s_cbranch_execz .LBB0_1256
	s_and_b64 s[6:7], s[88:89], exec
	s_andn2_saveexec_b64 s[8:9], s[0:1]
	s_cbranch_execnz .LBB0_1257

.LBB0_1020:
	v_cndmask_b32_e64 v1, 0, 1, s[34:35]
	s_mov_b64 s[76:77], 0
	v_cmp_ne_u32_e64 s[26:27], 1, v1
	s_andn2_b64 vcc, exec, s[34:35]
	s_mov_b64 s[34:35], s[96:97]
	s_cbranch_vccnz .LBB0_1063
	v_mov_b32_e32 v1, -1
	v_mov_b32_e32 v2, -1
	s_and_saveexec_b64 s[0:1], s[92:93]
	ds_read_b32 v2, v215 offset:8704
	s_or_b64 exec, exec, s[0:1]
	s_and_saveexec_b64 s[0:1], s[24:25]
	ds_read_b32 v1, v215 offset:8960
	s_or_b64 exec, exec, s[0:1]
	v_mov_b32_e32 v5, 30
	v_mov_b32_e32 v4, 0
	s_mov_b32 s98, 0
	s_mov_b32 s99, 30
	s_waitcnt lgkmcnt(0)

.Ltk_done_1:
	v_mov_b32_e32 v4, s98
	v_cmp_gt_i32_e64 s[28:29], v2, v4
	s_bcnt1_i32_b64 s6, s[28:29]
	v_cmp_gt_i32_e64 s[28:29], v1, v4
	s_bcnt1_i32_b64 s7, s[28:29]
	s_add_i32 s6, s6, s7
	v_cmp_ne_u32_e64 s[0:1], v2, v4
	v_cmp_eq_u32_e64 s[30:31], v2, v4
	v_cmp_eq_u32_e32 vcc, v1, v4
	v_cmp_le_i32_e64 s[36:37], v2, v4
	s_sub_i32 s44, 13, s6
	s_mov_b64 s[6:7], -1
	s_and_saveexec_b64 s[34:35], s[36:37]
	s_cbranch_execz .LBB0_1033
	s_mov_b64 s[6:7], 0
	s_and_saveexec_b64 s[8:9], s[0:1]
	s_xor_b64 s[0:1], exec, s[8:9]
	s_cbranch_execz .LBB0_1258
	s_and_b64 s[6:7], s[88:89], exec
	s_andn2_saveexec_b64 s[8:9], s[0:1]
	s_cbranch_execnz .LBB0_1259

.LBB0_1035:
	v_mov_b32_e32 v1, -1
	v_mov_b32_e32 v2, -1
	s_and_saveexec_b64 s[0:1], s[92:93]
	ds_read_b32 v2, v215 offset:9728
	s_or_b64 exec, exec, s[0:1]
	s_and_saveexec_b64 s[0:1], s[24:25]
	ds_read_b32 v1, v215 offset:9984
	s_or_b64 exec, exec, s[0:1]
	v_mov_b32_e32 v5, 30
	v_mov_b32_e32 v4, 0
	s_mov_b32 s98, 0
	s_mov_b32 s99, 30
	s_waitcnt lgkmcnt(0)

.Ltk_done_2:
	v_mov_b32_e32 v4, s98
	v_cmp_gt_i32_e64 s[28:29], v2, v4
	s_bcnt1_i32_b64 s6, s[28:29]
	v_cmp_gt_i32_e64 s[28:29], v1, v4
	s_bcnt1_i32_b64 s7, s[28:29]
	s_add_i32 s6, s6, s7
	v_cmp_ne_u32_e64 s[0:1], v2, v4
	v_cmp_eq_u32_e64 s[30:31], v2, v4
	v_cmp_eq_u32_e32 vcc, v1, v4
	v_cmp_le_i32_e64 s[36:37], v2, v4
	s_sub_i32 s46, 13, s6
	s_mov_b64 s[6:7], -1
	s_and_saveexec_b64 s[44:45], s[36:37]
	s_cbranch_execz .LBB0_1047
	s_mov_b64 s[6:7], 0
	s_and_saveexec_b64 s[8:9], s[0:1]
	s_xor_b64 s[0:1], exec, s[8:9]
	s_cbranch_execz .LBB0_1260
	s_and_b64 s[6:7], s[88:89], exec
	s_andn2_saveexec_b64 s[8:9], s[0:1]
	s_cbranch_execnz .LBB0_1261

.LBB0_1049:
	v_mov_b32_e32 v1, -1
	v_mov_b32_e32 v2, -1
	s_and_saveexec_b64 s[0:1], s[92:93]
	ds_read_b32 v2, v215 offset:10752
	s_or_b64 exec, exec, s[0:1]
	s_and_saveexec_b64 s[0:1], s[24:25]
	ds_read_b32 v1, v215 offset:11008
	s_or_b64 exec, exec, s[0:1]
	v_mov_b32_e32 v5, 30
	v_mov_b32_e32 v4, 0
	s_mov_b32 s98, 0
	s_mov_b32 s99, 30
	s_waitcnt lgkmcnt(0)

.Ltk_done_3:
	v_mov_b32_e32 v4, s98
	v_cmp_gt_i32_e64 s[28:29], v2, v4
	s_bcnt1_i32_b64 s6, s[28:29]
	v_cmp_gt_i32_e64 s[28:29], v1, v4
	s_bcnt1_i32_b64 s7, s[28:29]
	s_add_i32 s6, s6, s7
	v_cmp_ne_u32_e64 s[0:1], v2, v4
	v_cmp_eq_u32_e64 s[30:31], v2, v4
	v_cmp_eq_u32_e32 vcc, v1, v4
	v_cmp_le_i32_e64 s[36:37], v2, v4
	s_sub_i32 s90, 13, s6
	s_mov_b64 s[6:7], -1
	s_and_saveexec_b64 s[60:61], s[36:37]
	s_cbranch_execz .LBB0_1061
	s_mov_b64 s[6:7], 0
	s_and_saveexec_b64 s[8:9], s[0:1]
	s_xor_b64 s[0:1], exec, s[8:9]
	s_cbranch_execz .LBB0_1262
	s_and_b64 s[6:7], s[88:89], exec
	s_andn2_saveexec_b64 s[8:9], s[0:1]
	s_cbranch_execnz .LBB0_1263

.LBB0_1064:
	v_mov_b32_e32 v1, -1
	v_mov_b32_e32 v2, -1
	s_and_saveexec_b64 s[0:1], s[92:93]
	ds_read_b32 v2, v215 offset:9216
	s_or_b64 exec, exec, s[0:1]
	s_and_saveexec_b64 s[0:1], s[24:25]
	ds_read_b32 v1, v215 offset:9472
	s_or_b64 exec, exec, s[0:1]
	v_mov_b32_e32 v5, 30
	v_mov_b32_e32 v4, 0
	s_mov_b32 s98, 0
	s_mov_b32 s99, 30
	s_waitcnt lgkmcnt(0)

.LBB0_1078:
	v_mov_b32_e32 v1, -1
	v_mov_b32_e32 v2, -1
	s_and_saveexec_b64 s[0:1], s[92:93]
	ds_read_b32 v2, v215 offset:10240
	s_or_b64 exec, exec, s[0:1]
	s_and_saveexec_b64 s[0:1], s[24:25]
	ds_read_b32 v1, v215 offset:10496
	s_or_b64 exec, exec, s[0:1]
	v_mov_b32_e32 v5, 30
	v_mov_b32_e32 v4, 0
	s_mov_b32 s98, 0
	s_mov_b32 s99, 30
	s_waitcnt lgkmcnt(0)

.Ltk_done_5:
	v_mov_b32_e32 v4, s98
	v_cmp_gt_i32_e64 s[28:29], v2, v4
	s_bcnt1_i32_b64 s6, s[28:29]
	v_cmp_gt_i32_e64 s[28:29], v1, v4
	s_bcnt1_i32_b64 s7, s[28:29]
	s_add_i32 s6, s6, s7
	v_cmp_ne_u32_e64 s[0:1], v2, v4
	v_cmp_eq_u32_e64 s[30:31], v2, v4
	v_cmp_eq_u32_e32 vcc, v1, v4
	v_cmp_le_i32_e64 s[36:37], v2, v4
	s_sub_i32 s52, 13, s6
	s_mov_b64 s[6:7], -1
	s_and_saveexec_b64 s[50:51], s[36:37]
	s_cbranch_execz .LBB0_1090
	s_mov_b64 s[6:7], 0
	s_and_saveexec_b64 s[8:9], s[0:1]
	s_xor_b64 s[0:1], exec, s[8:9]
	s_cbranch_execz .LBB0_1266
	s_and_b64 s[6:7], s[88:89], exec
	s_andn2_saveexec_b64 s[8:9], s[0:1]
	s_cbranch_execnz .LBB0_1267

.LBB0_1092:
	v_mov_b32_e32 v1, -1
	v_mov_b32_e32 v2, -1
	s_and_saveexec_b64 s[0:1], s[92:93]
	ds_read_b32 v2, v215 offset:11264
	s_or_b64 exec, exec, s[0:1]
	s_and_saveexec_b64 s[0:1], s[24:25]
	ds_read_b32 v1, v215 offset:11520
	s_or_b64 exec, exec, s[0:1]
	v_mov_b32_e32 v5, 30
	v_mov_b32_e32 v4, 0
	s_mov_b32 s98, 0
	s_mov_b32 s99, 30
	s_waitcnt lgkmcnt(0)

.Ltk_done_6:
	v_mov_b32_e32 v4, s98
	v_cmp_gt_i32_e64 s[28:29], v2, v4
	s_bcnt1_i32_b64 s6, s[28:29]
	v_cmp_gt_i32_e64 s[28:29], v1, v4
	s_bcnt1_i32_b64 s7, s[28:29]
	s_add_i32 s6, s6, s7
	v_cmp_ne_u32_e64 s[0:1], v2, v4
	v_cmp_eq_u32_e64 s[30:31], v2, v4
	v_cmp_eq_u32_e32 vcc, v1, v4
	v_cmp_le_i32_e64 s[36:37], v2, v4
	s_sub_i32 s84, 13, s6
	s_mov_b64 s[8:9], -1
	s_and_saveexec_b64 s[6:7], s[36:37]
	s_cbranch_execz .LBB0_1104
	s_mov_b64 s[36:37], 0
	s_and_saveexec_b64 s[8:9], s[0:1]
	s_xor_b64 s[0:1], exec, s[8:9]
	s_cbranch_execz .LBB0_1268
	s_and_b64 s[36:37], s[88:89], exec
	s_andn2_saveexec_b64 s[8:9], s[0:1]
	s_cbranch_execnz .LBB0_1269

.LBB0_1105:
	v_mov_b32_e32 v1, -1
	v_mov_b32_e32 v2, -1
	s_and_saveexec_b64 s[0:1], s[92:93]
	ds_read_b32 v2, v215 offset:11776
	s_or_b64 exec, exec, s[0:1]
	s_and_saveexec_b64 s[0:1], s[24:25]
	ds_read_b32 v1, v215 offset:12032
	s_or_b64 exec, exec, s[0:1]
	v_mov_b32_e32 v5, 30
	v_mov_b32_e32 v4, 0
	s_mov_b32 s98, 0
	s_mov_b32 s99, 30
	s_waitcnt lgkmcnt(0)

.Ltk_done_7:
	v_mov_b32_e32 v4, s98
	v_cmp_gt_i32_e64 s[24:25], v2, v4
	s_bcnt1_i32_b64 s6, s[24:25]
	v_cmp_gt_i32_e64 s[24:25], v1, v4
	s_bcnt1_i32_b64 s7, s[24:25]
	s_add_i32 s6, s6, s7
	v_cmp_ne_u32_e64 s[0:1], v2, v4
	v_cmp_eq_u32_e64 s[26:27], v2, v4
	v_cmp_eq_u32_e32 vcc, v1, v4
	v_cmp_le_i32_e64 s[28:29], v2, v4
	s_sub_i32 s84, 13, s6
	s_mov_b64 s[8:9], -1
	s_and_saveexec_b64 s[6:7], s[28:29]
	s_cbranch_execz .LBB0_1117
	s_mov_b64 s[28:29], 0
	s_and_saveexec_b64 s[8:9], s[0:1]
	s_xor_b64 s[0:1], exec, s[8:9]
	s_cbranch_execz .LBB0_1270
	s_and_b64 s[28:29], s[88:89], exec
	s_andn2_saveexec_b64 s[8:9], s[0:1]
	s_cbranch_execnz .LBB0_1271
